# baseline (speedup 1.0000x reference)
_Z8k_stageAPKfS0_S0_S0_PDF16_PKDF16_S0_S1_ii:
	s_load_dwordx2 s[86:87], s[0:1], 0x30
	s_load_dwordx2 s[82:83], s[0:1], 0x40
	s_mov_b32 s81, s3
	s_load_dwordx2 s[64:65], s[0:1], 0x40
	v_readfirstlane_b32 s94, v0
	s_nop 0
	s_lshr_b32 s94, s94, 6
	s_load_dwordx8 s[4:11], s[0:1], 0x0
	v_readfirstlane_b32 s14, v0
	s_lshr_b32 s15, s2, 5
	s_lshl_b32 s2, s2, 7
	s_lshr_b32 s20, s14, 6
	s_and_b32 s12, s2, 0xf80
	s_lshl_b32 s13, s15, 12
	s_mov_b32 s18, s3
	s_cmpk_lt_u32 s14, 0x100
	s_waitcnt lgkmcnt(0)
	s_cselect_b32 s2, s4, s6
	s_cselect_b32 s3, s5, s7
	s_cselect_b32 s4, s8, s10
	s_cselect_b32 s5, s9, s11
	s_cmp_eq_u32 s18, 0
	s_cselect_b32 s3, s3, s5
	s_cselect_b32 s2, s2, s4
	s_lshr_b32 s5, s14, 1
	s_lshl_b32 s4, s15, 7
	s_and_b32 s5, s5, 0x60
	v_bfe_u32 v1, v0, 5, 1
	s_or_b32 s4, s5, s4
	v_lshl_or_b32 v82, v1, 3, s4
	v_mov_b32_e32 v83, 0
	v_lshlrev_b64 v[2:3], 14, v[82:83]
	v_lshlrev_b32_e32 v78, 2, v0
	s_mov_b32 s17, 0
	v_lshl_add_u64 v[2:3], s[2:3], 0, v[2:3]
	s_lshl_b32 s16, s12, 2
	v_and_b32_e32 v79, 0x7c, v78
	v_lshl_add_u64 v[2:3], v[2:3], 0, s[16:17]
	v_lshlrev_b32_e32 v82, 2, v79
	v_lshl_add_u64 v[42:43], v[2:3], 0, v[82:83]
	s_movk_i32 s21, 0x4000
	v_add_co_u32_e32 v10, vcc, s21, v42
	s_mov_b32 s2, 0x8000
	s_nop 0
	v_addc_co_u32_e32 v11, vcc, 0, v43, vcc
	v_add_co_u32_e32 v18, vcc, s2, v42
	s_mov_b32 s2, 0xc000
	s_nop 0
	v_addc_co_u32_e32 v19, vcc, 0, v43, vcc
	v_add_co_u32_e32 v20, vcc, s2, v42
	s_mov_b32 s14, 0x10000
	s_nop 0
	v_addc_co_u32_e32 v21, vcc, 0, v43, vcc
	v_add_co_u32_e32 v26, vcc, s14, v42
	s_mov_b32 s2, 0x14000
	s_nop 0
	v_addc_co_u32_e32 v27, vcc, 0, v43, vcc
	v_add_co_u32_e32 v28, vcc, s2, v42
	s_mov_b32 s2, 0x18000
	s_nop 0
	v_addc_co_u32_e32 v29, vcc, 0, v43, vcc
	v_add_co_u32_e32 v34, vcc, s2, v42
	s_mov_b32 s2, 0x1c000
	s_nop 0
	v_addc_co_u32_e32 v35, vcc, 0, v43, vcc
	v_add_co_u32_e32 v36, vcc, s2, v42
	s_mov_b32 s2, 0x40000
	s_nop 0
	v_addc_co_u32_e32 v37, vcc, 0, v43, vcc
	v_add_co_u32_e32 v66, vcc, s2, v42
	s_mov_b32 s2, 0x44000
	s_nop 0
	v_addc_co_u32_e32 v67, vcc, 0, v43, vcc
	v_add_co_u32_e32 v68, vcc, s2, v42
	s_mov_b32 s2, 0x48000
	s_nop 0
	v_addc_co_u32_e32 v69, vcc, 0, v43, vcc
	global_load_dwordx4 v[2:5], v[42:43], off nt
	global_load_dwordx4 v[6:9], v[10:11], off nt
	v_add_co_u32_e32 v44, vcc, s2, v42
	global_load_dwordx4 v[10:13], v[18:19], off nt
	global_load_dwordx4 v[14:17], v[20:21], off nt
	s_nop 0
	global_load_dwordx4 v[18:21], v[26:27], off nt
	global_load_dwordx4 v[22:25], v[28:29], off nt
	s_nop 0
	global_load_dwordx4 v[26:29], v[34:35], off nt
	global_load_dwordx4 v[30:33], v[36:37], off nt
	v_addc_co_u32_e32 v45, vcc, 0, v43, vcc
	s_mov_b32 s2, 0x4c000
	v_add_co_u32_e32 v46, vcc, s2, v42
	s_mov_b32 s2, 0x50000
	s_nop 0
	v_addc_co_u32_e32 v47, vcc, 0, v43, vcc
	v_add_co_u32_e32 v70, vcc, s2, v42
	s_mov_b32 s2, 0x54000
	s_nop 0
	v_addc_co_u32_e32 v71, vcc, 0, v43, vcc
	v_add_co_u32_e32 v72, vcc, s2, v42
	s_mov_b32 s2, 0x58000
	s_nop 0
	v_addc_co_u32_e32 v73, vcc, 0, v43, vcc
	v_add_co_u32_e32 v74, vcc, s2, v42
	s_mov_b32 s2, 0x5c000
	s_nop 0
	v_addc_co_u32_e32 v75, vcc, 0, v43, vcc
	v_add_co_u32_e32 v76, vcc, s2, v42
	global_load_dwordx4 v[34:37], v[44:45], off nt
	global_load_dwordx4 v[38:41], v[46:47], off nt
	v_addc_co_u32_e32 v77, vcc, 0, v43, vcc
	global_load_dwordx4 v[42:45], v[74:75], off nt
	global_load_dwordx4 v[46:49], v[76:77], off nt
	global_load_dwordx4 v[50:53], v[70:71], off nt
	global_load_dwordx4 v[54:57], v[72:73], off nt
	global_load_dwordx4 v[58:61], v[66:67], off nt
	global_load_dwordx4 v[62:65], v[68:69], off nt
	v_lshl_or_b32 v1, s20, 2, v1
	v_lshrrev_b32_e32 v70, 5, v0
	v_or_b32_e32 v141, 0x200, v0
	v_or_b32_e32 v142, 0x600, v0
	s_or_b32 s16, s13, s12
	s_ashr_i32 s19, s18, 31
	s_lshl_b64 s[12:13], s[16:17], 9
	s_mov_b32 s15, 0x20000
	v_or_b32_e32 v144, 0xa00, v0
	v_bfe_u32 v140, v0, 4, 2
	v_and_b32_e32 v145, 15, v0
	v_lshlrev_b32_e32 v220, 9, v145
	s_waitcnt vmcnt(14)
	v_cvt_pk_f16_f32 v66, v2, v6
	v_lshlrev_b32_e32 v6, 9, v79
	v_bitop3_b32 v2, v78, v1, 12 bitop3:0x6c
	s_waitcnt vmcnt(12)
	v_cvt_pk_f16_f32 v67, v10, v14
	s_waitcnt vmcnt(10)
	v_cvt_pk_f16_f32 v68, v18, v22
	s_waitcnt vmcnt(8)
	v_cvt_pk_f16_f32 v69, v26, v30
	v_lshl_add_u32 v2, v2, 4, v6
	ds_write_b128 v2, v[66:69]
	v_cvt_pk_f16_f32 v66, v3, v7
	v_or_b32_e32 v7, 1, v79
	v_lshlrev_b32_e32 v10, 9, v7
	v_bitop3_b32 v2, v7, v1, 13 bitop3:0x6c
	v_cvt_pk_f16_f32 v69, v27, v31
	v_cvt_pk_f16_f32 v68, v19, v23
	v_cvt_pk_f16_f32 v67, v11, v15
	v_lshl_add_u32 v2, v2, 4, v10
	ds_write_b128 v2, v[66:69]
	v_cvt_pk_f16_f32 v66, v4, v8
	v_or_b32_e32 v8, 2, v79
	v_lshlrev_b32_e32 v11, 9, v8
	v_bitop3_b32 v2, v8, v1, 14 bitop3:0x6c
	v_cvt_pk_f16_f32 v69, v28, v32
	v_cvt_pk_f16_f32 v68, v20, v24
	v_cvt_pk_f16_f32 v67, v12, v16
	v_lshl_add_u32 v2, v2, 4, v11
	v_cvt_pk_f16_f32 v12, v5, v9
	v_or_b32_e32 v9, 3, v79
	ds_write_b128 v2, v[66:69]
	v_lshlrev_b32_e32 v16, 9, v9
	v_bitop3_b32 v2, v9, v1, 15 bitop3:0x6c
	v_cvt_pk_f16_f32 v15, v29, v33
	v_cvt_pk_f16_f32 v14, v21, v25
	v_cvt_pk_f16_f32 v13, v13, v17
	v_lshl_add_u32 v2, v2, 4, v16
	v_or_b32_e32 v1, 2, v1
	ds_write_b128 v2, v[12:15]
	v_bitop3_b32 v12, v78, v1, 12 bitop3:0x6c
	s_waitcnt vmcnt(4)
	v_cvt_pk_f16_f32 v5, v42, v46
	s_waitcnt vmcnt(2)
	v_cvt_pk_f16_f32 v4, v50, v54
	v_cvt_pk_f16_f32 v3, v34, v38
	s_waitcnt vmcnt(0)
	v_cvt_pk_f16_f32 v2, v58, v62
	v_lshl_add_u32 v6, v12, 4, v6
	ds_write_b128 v6, v[2:5]
	v_bitop3_b32 v6, v7, v1, 13 bitop3:0x6c
	v_cvt_pk_f16_f32 v5, v43, v47
	v_cvt_pk_f16_f32 v4, v51, v55
	v_cvt_pk_f16_f32 v3, v35, v39
	v_cvt_pk_f16_f32 v2, v59, v63
	v_lshl_add_u32 v6, v6, 4, v10
	ds_write_b128 v6, v[2:5]
	v_bitop3_b32 v6, v8, v1, 14 bitop3:0x6c
	v_cvt_pk_f16_f32 v5, v44, v48
	v_cvt_pk_f16_f32 v4, v52, v56
	v_cvt_pk_f16_f32 v3, v36, v40
	v_cvt_pk_f16_f32 v2, v60, v64
	v_lshl_add_u32 v6, v6, 4, v11
	v_bitop3_b32 v1, v9, v1, 15 bitop3:0x6c
	ds_write_b128 v6, v[2:5]
	v_cvt_pk_f16_f32 v5, v45, v49
	v_cvt_pk_f16_f32 v4, v53, v57
	v_cvt_pk_f16_f32 v3, v37, v41
	v_cvt_pk_f16_f32 v2, v61, v65
	v_lshl_add_u32 v1, v1, 4, v16
	ds_write_b128 v1, v[2:5]
	v_bitop3_b32 v2, v70, v0, 31 bitop3:0x78
	v_lshlrev_b32_e32 v1, 9, v70
	v_lshlrev_b32_e32 v22, 4, v2
	v_or_b32_e32 v10, v22, v1
	s_waitcnt lgkmcnt(0)
	s_barrier
	s_mul_i32 s84, s81, s83
	s_add_i32 s84, s84, s82
	s_mul_i32 s84, s84, 0xc00
	s_add_u32 s88, s86, s84
	s_addc_u32 s89, s87, 0
	v_mbcnt_lo_u32_b32 v251, -1, 0
	v_mbcnt_hi_u32_b32 v251, -1, v251
	v_bfe_u32 v251, v251, 4, 2
	v_lshlrev_b32_e32 v251, 4, v251
	s_mul_i32 s85, s94, 0xc0
	v_add_u32_e32 v251, s85, v251
	global_load_dwordx4 v[252:255], v251, s[88:89]
	global_load_dwordx4 v[252:255], v251, s[88:89] offset:64
	global_load_dwordx4 v[252:255], v251, s[88:89] offset:128
	global_load_dwordx4 v[252:255], v251, s[88:89] offset:1536
	global_load_dwordx4 v[252:255], v251, s[88:89] offset:1600
	global_load_dwordx4 v[252:255], v251, s[88:89] offset:1664
	ds_read_b128 v[2:5], v10
	s_load_dwordx8 s[4:11], s[0:1], 0x20
	s_load_dwordx2 s[2:3], s[0:1], 0x40
	v_lshlrev_b32_e32 v24, 4, v0
	v_and_b32_e32 v25, 0x1e00, v24
	v_or_b32_e32 v26, v22, v25
	s_waitcnt lgkmcnt(0)
	v_pk_max_f16 v6, v5, v5
	v_and_b32_e32 v18, 31, v0
	v_pk_max_f16 v9, v6, 0
	v_pk_max_f16 v6, v4, v4
	v_lshlrev_b32_e32 v29, 4, v18
	v_pk_max_f16 v8, v6, 0
	v_pk_max_f16 v6, v3, v3
	s_lshl_b64 s[0:1], s[18:19], 23
	v_pk_max_f16 v7, v6, 0
	v_pk_max_f16 v6, v2, v2
	s_add_u32 s0, s4, s0
	v_pk_max_f16 v6, v6, 0
	ds_write_b128 v10, v[6:9]
	v_lshlrev_b32_e32 v6, 4, v141
	v_and_b32_e32 v23, 0x3e00, v6
	v_or_b32_e32 v14, v22, v23
	ds_read_b128 v[6:9], v14
	s_addc_u32 s1, s5, s1
	s_add_u32 s12, s0, s12
	s_addc_u32 s0, s1, s13
	s_and_b32 s13, s0, 0xffff
	s_waitcnt lgkmcnt(0)
	v_pk_max_f16 v10, v9, v9
	v_or_b32_e32 v1, v1, v29
	v_pk_max_f16 v13, v10, 0
	v_pk_max_f16 v10, v8, v8
	buffer_store_dwordx4 v[2:5], v1, s[12:15], 0 offen sc1
	v_pk_max_f16 v12, v10, 0
	v_pk_max_f16 v10, v7, v7
	v_or_b32_e32 v1, v23, v29
	v_pk_max_f16 v11, v10, 0
	v_pk_max_f16 v10, v6, v6
	buffer_store_dwordx4 v[6:9], v1, s[12:15], 0 offen sc1
	v_pk_max_f16 v10, v10, 0
	ds_write_b128 v14, v[10:13]
	ds_read_b128 v[10:13], v26 offset:16384
	v_or_b32_e32 v25, v25, v29
	v_or_b32_e32 v6, 0x4000, v25
	s_mov_b32 s0, 0xfe00
	s_waitcnt lgkmcnt(0)
	v_pk_max_f16 v14, v13, v13
	s_nop 0
	v_pk_max_f16 v17, v14, 0
	v_pk_max_f16 v14, v12, v12
	buffer_store_dwordx4 v[10:13], v6, s[12:15], 0 offen sc1
	v_pk_max_f16 v16, v14, 0
	v_pk_max_f16 v14, v11, v11
	s_nop 0
	v_pk_max_f16 v15, v14, 0
	v_pk_max_f16 v14, v10, v10
	s_nop 0
	v_pk_max_f16 v14, v14, 0
	ds_write_b128 v26, v[14:17] offset:16384
	v_lshlrev_b32_e32 v14, 4, v142
	v_and_b32_e32 v27, 0x7e00, v14
	v_or_b32_e32 v28, v22, v27
	ds_read_b128 v[14:17], v28
	v_or_b32_e32 v10, v27, v29
	s_waitcnt lgkmcnt(0)
	v_pk_max_f16 v18, v17, v17
	s_nop 0
	v_pk_max_f16 v21, v18, 0
	v_pk_max_f16 v18, v16, v16
	buffer_store_dwordx4 v[14:17], v10, s[12:15], 0 offen sc1
	v_pk_max_f16 v20, v18, 0
	v_pk_max_f16 v18, v15, v15
	v_or_b32_e32 v10, 0x8000, v25
	v_pk_max_f16 v19, v18, 0
	v_pk_max_f16 v18, v14, v14
	s_nop 0
	v_pk_max_f16 v18, v18, 0
	ds_write_b128 v28, v[18:21]
	ds_read_b128 v[18:21], v26 offset:32768
	s_waitcnt lgkmcnt(0)
	v_pk_max_f16 v1, v21, v21
	s_nop 0
	v_pk_max_f16 v5, v1, 0
	v_pk_max_f16 v1, v20, v20
	buffer_store_dwordx4 v[18:21], v10, s[12:15], 0 offen sc1
	v_pk_max_f16 v4, v1, 0
	v_pk_max_f16 v1, v19, v19
	s_nop 0
	v_pk_max_f16 v3, v1, 0
	v_pk_max_f16 v1, v18, v18
	s_nop 0
	v_pk_max_f16 v2, v1, 0
	v_lshlrev_b32_e32 v1, 4, v144
	v_and_b32_e32 v1, 0xbe00, v1
	ds_write_b128 v26, v[2:5] offset:32768
	v_or_b32_e32 v23, v22, v1
	ds_read_b128 v[2:5], v23
	v_or_b32_e32 v1, v1, v29
	s_waitcnt lgkmcnt(0)
	v_pk_max_f16 v6, v5, v5
	s_nop 0
	v_pk_max_f16 v9, v6, 0
	v_pk_max_f16 v6, v4, v4
	buffer_store_dwordx4 v[2:5], v1, s[12:15], 0 offen sc1
	v_pk_max_f16 v8, v6, 0
	v_pk_max_f16 v6, v3, v3
	v_or_b32_e32 v1, 0xc000, v25
	v_pk_max_f16 v7, v6, 0
	v_pk_max_f16 v6, v2, v2
	s_nop 0
	v_pk_max_f16 v6, v6, 0
	ds_write_b128 v23, v[6:9]
	ds_read_b128 v[6:9], v26 offset:49152
	s_waitcnt lgkmcnt(0)
	v_pk_max_f16 v10, v9, v9
	s_nop 0
	v_pk_max_f16 v13, v10, 0
	v_pk_max_f16 v10, v8, v8
	buffer_store_dwordx4 v[6:9], v1, s[12:15], 0 offen sc1
	v_pk_max_f16 v12, v10, 0
	v_pk_max_f16 v10, v7, v7
	s_nop 0
	v_pk_max_f16 v11, v10, 0
	v_pk_max_f16 v10, v6, v6
	s_nop 0
	v_pk_max_f16 v10, v10, 0
	ds_write_b128 v26, v[10:13] offset:49152
	v_mov_b32_e32 v10, 0xe000
	v_bitop3_b32 v14, v24, s0, v10 bitop3:0xc8
	s_mul_i32 s0, s3, s18
	v_or_b32_e32 v15, v22, v14
	s_add_i32 s0, s0, s2
	ds_read_b128 v[10:13], v15
	s_mul_i32 s2, s0, 0x60000
	s_mul_hi_i32 s1, s0, 0x60000
	s_add_u32 s2, s6, s2
	s_mulk_i32 s0, 0x300
	s_addc_u32 s3, s7, s1
	s_ashr_i32 s1, s0, 31
	s_lshl_b64 s[0:1], s[0:1], 2
	v_or_b32_e32 v1, v14, v29
	s_add_u32 s4, s8, s0
	s_waitcnt lgkmcnt(0)
	buffer_store_dwordx4 v[10:13], v1, s[12:15], 0 offen sc1
	v_pk_max_f16 v1, v13, v13
	s_addc_u32 s5, s9, s1
	s_mul_i32 s0, s18, 0x1800000
	v_pk_max_f16 v5, v1, 0
	v_pk_max_f16 v1, v12, v12
	s_mul_hi_i32 s1, s18, 0x1800000
	s_add_u32 s0, s10, s0
	v_pk_max_f16 v4, v1, 0
	v_pk_max_f16 v1, v11, v11
	s_addc_u32 s1, s11, s1
	v_pk_max_f16 v3, v1, 0
	v_pk_max_f16 v1, v10, v10
	s_and_b32 s1, s1, 0xffff
	s_mul_i32 s7, s20, 0x6000
	v_pk_max_f16 v2, v1, 0
	v_and_b32_e32 v1, 63, v0
	s_mul_hi_u32 s6, s20, 0x6000
	s_add_u32 s2, s2, s7
	s_addc_u32 s3, s3, s6
	v_lshlrev_b32_e32 v82, 4, v1
	v_lshl_add_u64 v[118:119], s[2:3], 0, v[82:83]
	s_movk_i32 s6, 0x1000
	v_add_co_u32_e32 v50, vcc, s6, v118
	s_movk_i32 s6, 0x2000
	s_nop 0
	v_addc_co_u32_e32 v51, vcc, 0, v119, vcc
	ds_write_b128 v15, v[2:5]
	v_add_co_u32_e32 v52, vcc, s6, v118
	global_load_dwordx4 v[2:5], v82, s[2:3] offset:1024
	global_load_dwordx4 v[6:9], v82, s[2:3] offset:2048
	v_addc_co_u32_e32 v53, vcc, 0, v119, vcc
	global_load_dwordx4 v[10:13], v82, s[2:3] offset:3072
	global_load_dwordx4 v[14:17], v[52:53], off offset:-4096
	global_load_dwordx4 v[18:21], v[50:51], off offset:1024
	global_load_dwordx4 v[22:25], v[50:51], off offset:2048
	global_load_dwordx4 v[26:29], v82, s[2:3]
	global_load_dwordx4 v[30:33], v[50:51], off offset:3072
	global_load_dwordx4 v[34:37], v[52:53], off
	global_load_dwordx4 v[38:41], v[52:53], off offset:1024
	global_load_dwordx4 v[42:45], v[52:53], off offset:2048
	global_load_dwordx4 v[46:49], v[52:53], off offset:3072
	s_movk_i32 s2, 0x3000
	v_add_co_u32_e32 v116, vcc, s2, v118
	s_waitcnt lgkmcnt(0)
	s_nop 0
	v_addc_co_u32_e32 v117, vcc, 0, v119, vcc
	v_add_co_u32_e32 v132, vcc, s21, v118
	s_barrier
	s_cmp_lt_u32 s94, 4
	s_cbranch_scc1 .Lmystag1_2
	s_sleep 7

	.amdhsa_kernel _Z8k_stageAPKfS0_S0_S0_PDF16_PKDF16_S0_S1_ii
		.amdhsa_group_segment_fixed_size 115712
		.amdhsa_private_segment_fixed_size 0
		.amdhsa_kernarg_size 72
		.amdhsa_user_sgpr_count 2
		.amdhsa_user_sgpr_dispatch_ptr 0
		.amdhsa_user_sgpr_queue_ptr 0
		.amdhsa_user_sgpr_kernarg_segment_ptr 1
		.amdhsa_user_sgpr_dispatch_id 0
		.amdhsa_user_sgpr_kernarg_preload_length 0
		.amdhsa_user_sgpr_kernarg_preload_offset 0
		.amdhsa_user_sgpr_private_segment_size 0
		.amdhsa_uses_dynamic_stack 0
		.amdhsa_enable_private_segment 0
		.amdhsa_system_sgpr_workgroup_id_x 1
		.amdhsa_system_sgpr_workgroup_id_y 1
		.amdhsa_system_sgpr_workgroup_id_z 0
		.amdhsa_system_sgpr_workgroup_info 0
		.amdhsa_system_vgpr_workitem_id 0
		.amdhsa_next_free_vgpr 256
		.amdhsa_next_free_sgpr 96
		.amdhsa_accum_offset 256
		.amdhsa_reserve_vcc 1
		.amdhsa_float_round_mode_32 0
		.amdhsa_float_round_mode_16_64 0
		.amdhsa_float_denorm_mode_32 3
		.amdhsa_float_denorm_mode_16_64 3
		.amdhsa_dx10_clamp 1
		.amdhsa_ieee_mode 1
		.amdhsa_fp16_overflow 0
		.amdhsa_tg_split 0
		.amdhsa_exception_fp_ieee_invalid_op 0
		.amdhsa_exception_fp_denorm_src 0
		.amdhsa_exception_fp_ieee_div_zero 0
		.amdhsa_exception_fp_ieee_overflow 0
		.amdhsa_exception_fp_ieee_underflow 0
		.amdhsa_exception_fp_ieee_inexact 0
		.amdhsa_exception_int_div_zero 0
	.end_amdhsa_kernel

_Z7k_stageILi0ELi8EEv8AttnArgsPKDF16_PKfPDF16_iii:
	s_load_dwordx2 s[86:87], s[0:1], 0x78
	s_load_dwordx2 s[82:83], s[0:1], 0x88
	s_mov_b32 s81, s3
	s_load_dwordx16 s[64:79], s[0:1], 0x40
	s_load_dwordx16 s[64:79], s[0:1], 0x0
	v_readfirstlane_b32 s94, v0
	s_nop 0
	s_lshr_b32 s94, s94, 6
	s_load_dwordx4 s[8:11], s[0:1], 0x88
	s_lshl_b32 s4, s2, 4
	s_and_b32 s4, s4, 0x70
	s_lshr_b32 s5, s2, 3
	s_add_i32 s4, s4, s5
	s_lshr_b32 s7, s4, 5
	s_lshl_b32 s6, s4, 1
	s_waitcnt lgkmcnt(0)
	s_lshl_b32 s11, s2, 1
	s_cmp_gt_i32 s10, 0
	v_readfirstlane_b32 s24, v0
	s_cbranch_scc1 .LBB3_2
	s_lshl_b32 s31, s7, 12
	s_ashr_i32 s2, s3, 31
	s_mov_b64 s[4:5], 0
	s_branch .LBB3_3

.LBB3_82:
	s_mul_i32 s84, s81, s83
	s_add_i32 s84, s84, s82
	s_mul_i32 s84, s84, 0xc00
	s_add_u32 s88, s86, s84
	s_addc_u32 s89, s87, 0
	v_mbcnt_lo_u32_b32 v251, -1, 0
	v_mbcnt_hi_u32_b32 v251, -1, v251
	v_bfe_u32 v251, v251, 4, 2
	v_lshlrev_b32_e32 v251, 4, v251
	s_mul_i32 s85, s94, 0xc0
	v_add_u32_e32 v251, s85, v251
	global_load_dwordx4 v[252:255], v251, s[88:89]
	global_load_dwordx4 v[252:255], v251, s[88:89] offset:64
	global_load_dwordx4 v[252:255], v251, s[88:89] offset:128
	global_load_dwordx4 v[252:255], v251, s[88:89] offset:1536
	global_load_dwordx4 v[252:255], v251, s[88:89] offset:1600
	global_load_dwordx4 v[252:255], v251, s[88:89] offset:1664
	s_mul_i32 s0, s9, s3
	s_lshl_b32 s1, s30, 6
	s_add_i32 s0, s0, s8
	s_or_b32 s1, s1, s31
	s_or_b32 s7, s1, s11
	s_mul_i32 s4, s0, 0x60000
	s_mul_hi_i32 s1, s0, 0x60000
	s_waitcnt lgkmcnt(0)
	s_add_u32 s6, s12, s4
	s_mulk_i32 s0, 0x300
	s_addc_u32 s8, s13, s1
	s_ashr_i32 s1, s0, 31
	s_lshl_b64 s[0:1], s[0:1], 2
	s_add_u32 s4, s14, s0
	s_addc_u32 s5, s15, s1
	s_mul_i32 s0, s2, 0x1800000
	s_mul_hi_u32 s1, s3, 0x1800000
	s_add_i32 s1, s1, s0
	s_mul_i32 s0, s3, 0x1800000
	s_add_u32 s0, s20, s0
	v_readfirstlane_b32 s2, v0
	s_addc_u32 s1, s21, s1
	s_lshr_b32 s9, s2, 6
	s_and_b32 s1, s1, 0xffff
	s_mul_i32 s2, s9, 0x6000
	v_and_b32_e32 v2, 63, v0
	s_mul_hi_u32 s3, s9, 0x6000
	s_add_u32 s2, s6, s2
	s_addc_u32 s3, s8, s3
	v_lshlrev_b32_e32 v82, 4, v2
	v_mov_b32_e32 v83, 0
	v_lshl_add_u64 v[118:119], s[2:3], 0, v[82:83]
	s_movk_i32 s6, 0x1000
	v_add_co_u32_e32 v50, vcc, s6, v118
	s_movk_i32 s6, 0x2000
	s_nop 0
	v_addc_co_u32_e32 v51, vcc, 0, v119, vcc
	v_add_co_u32_e32 v52, vcc, s6, v118
	global_load_dwordx4 v[2:5], v82, s[2:3] offset:1024
	global_load_dwordx4 v[6:9], v82, s[2:3] offset:2048
	v_addc_co_u32_e32 v53, vcc, 0, v119, vcc
	global_load_dwordx4 v[10:13], v82, s[2:3] offset:3072
	global_load_dwordx4 v[14:17], v[52:53], off offset:-4096
	global_load_dwordx4 v[18:21], v[50:51], off offset:1024
	global_load_dwordx4 v[22:25], v[50:51], off offset:2048
	global_load_dwordx4 v[26:29], v82, s[2:3]
	global_load_dwordx4 v[30:33], v[50:51], off offset:3072
	global_load_dwordx4 v[34:37], v[52:53], off
	global_load_dwordx4 v[38:41], v[52:53], off offset:1024
	global_load_dwordx4 v[42:45], v[52:53], off offset:2048
	global_load_dwordx4 v[46:49], v[52:53], off offset:3072
	s_movk_i32 s2, 0x3000
	v_add_co_u32_e32 v116, vcc, s2, v118
	s_movk_i32 s2, 0x4000
	s_nop 0
	v_addc_co_u32_e32 v117, vcc, 0, v119, vcc
	v_add_co_u32_e32 v156, vcc, s2, v118
	s_nop 1
	v_addc_co_u32_e32 v157, vcc, 0, v119, vcc
	s_barrier
	s_cmp_lt_u32 s94, 4
	s_cbranch_scc1 .Lmystag3_1
	s_sleep 7

_Z7k_stageILi1ELi4EEv8AttnArgsPKDF16_PKfPDF16_iii:
	s_load_dwordx2 s[86:87], s[0:1], 0x78
	s_load_dwordx2 s[82:83], s[0:1], 0x88
	s_mov_b32 s81, s3
	s_load_dwordx16 s[64:79], s[0:1], 0x0
	v_readfirstlane_b32 s94, v0
	s_nop 0
	s_lshr_b32 s94, s94, 6
	s_load_dwordx4 s[28:31], s[0:1], 0x70
	s_load_dwordx2 s[24:25], s[0:1], 0x80
	s_load_dword s33, s[0:1], 0x90
	s_lshl_b32 s4, s2, 5
	s_and_b32 s45, s4, 0xe0
	s_lshr_b32 s4, s2, 3
	s_add_i32 s45, s45, s4
	s_and_b32 s44, s2, 56
	v_readfirstlane_b32 s3, v0
	v_and_b32_e32 v1, 15, v0
	s_waitcnt lgkmcnt(0)
	s_cmp_lt_i32 s33, 1
	v_bfe_u32 v167, v0, 4, 2
	s_cbranch_scc1 .LBB4_155
	s_lshr_b32 s2, s3, 2
	v_lshrrev_b32_e32 v7, 7, v0
	v_lshrrev_b32_e32 v2, 5, v0
	v_lshrrev_b32_e32 v3, 4, v0
	s_and_b32 s2, s2, 16
	v_lshrrev_b32_e32 v4, 6, v0
	v_and_b32_e32 v7, 1, v7
	v_and_b32_e32 v2, 4, v2
	v_or_b32_e32 v179, s2, v1
	v_and_b32_e32 v5, 4, v4
	s_load_dwordx2 s[40:41], s[0:1], 0x60
	s_bitcmp1_b32 s3, 6
	v_lshlrev_b16_e32 v7, 2, v7
	v_and_b32_e32 v8, 3, v3
	s_load_dwordx4 s[36:39], s[0:1], 0x0
	s_load_dwordx2 s[4:5], s[0:1], 0x10
	s_load_dwordx8 s[8:15], s[0:1], 0x18
	s_load_dwordx2 s[6:7], s[0:1], 0x38
	s_load_dwordx8 s[16:23], s[0:1], 0x40
	v_or_b32_e32 v178, v2, v167
	v_and_or_b32 v180, s45, 56, v5
	s_cselect_b64 s[26:27], -1, 0
	s_and_b32 s3, s45, 0x3ffffc0
	v_bitop3_b16 v3, v7, v3, 3 bitop3:0xf8
	v_bitop3_b16 v7, v7, 8, v8 bitop3:0xfe
	v_lshlrev_b32_e32 v8, 12, v5
	v_bitop3_b32 v2, v2, v179, v167 bitop3:0x36
	v_or_b32_e32 v6, s3, v180
	s_and_b32 s3, s45, 0x1ffc0
	v_and_b32_e32 v3, 0xffff, v3
	v_lshl_or_b32 v184, v2, 4, v8
	v_lshlrev_b32_e32 v2, 3, v5
	v_mov_b32_e32 v169, 0
	v_lshlrev_b32_e32 v168, 5, v179
	v_lshlrev_b32_e32 v181, 6, v6
	v_or_b32_e32 v6, s3, v180
	v_and_b32_e32 v7, 0xffff, v7
	v_or_b32_e32 v186, 8, v2
	v_or_b32_e32 v188, 16, v2
	v_bitop3_b32 v2, s2, v3, v1 bitop3:0x36
	v_lshlrev_b32_e32 v166, 3, v179
	s_waitcnt lgkmcnt(0)
	v_lshl_add_u64 v[170:171], s[38:39], 0, v[168:169]
	s_mov_b32 s39, 0x20000
	v_lshlrev_b32_e32 v189, 4, v2
	v_bitop3_b32 v2, s2, v7, v1 bitop3:0x36
	v_lshlrev_b32_e32 v193, 15, v6
	v_lshl_add_u64 v[172:173], s[4:5], 0, v[168:169]
	s_and_b32 s37, s37, 0xffff
	s_mov_b32 s38, 0x1800000
	v_add_u32_e32 v182, -1, v180
	v_add_u32_e32 v183, 4, v180
	v_lshl_add_u64 v[174:175], s[14:15], 0, v[168:169]
	v_lshl_add_u64 v[176:177], s[6:7], 0, v[168:169]
	s_and_b32 s13, s13, 0xffff
	s_mov_b32 s42, 0x800000
	s_mov_b32 s43, s39
	s_and_b32 s41, s41, 0xffff
	v_or_b32_e32 v185, 64, v181
	v_or_b32_e32 v187, 0x80, v181
	v_or_b32_e32 v190, 0xc0, v181
	v_lshl_or_b32 v191, v4, 3, 24
	v_lshlrev_b32_e32 v192, 4, v2
	v_lshlrev_b32_e32 v194, 4, v179
	v_or_b32_e32 v195, 0x8000, v193
	v_or_b32_e32 v196, 0x10000, v193
	v_or_b32_e32 v197, 0x18000, v193
	s_mov_b32 s46, 0
	s_movk_i32 s47, 0x300
	v_lshlrev_b32_e32 v198, 1, v166
	s_branch .LBB4_4

.LBB4_155:
	s_mul_i32 s84, s81, s83
	s_add_i32 s84, s84, s82
	s_mul_i32 s84, s84, 0xc00
	s_add_u32 s88, s86, s84
	s_addc_u32 s89, s87, 0
	v_mbcnt_lo_u32_b32 v251, -1, 0
	v_mbcnt_hi_u32_b32 v251, -1, v251
	v_bfe_u32 v251, v251, 4, 2
	v_lshlrev_b32_e32 v251, 4, v251
	s_mul_i32 s85, s94, 0xc0
	v_add_u32_e32 v251, s85, v251
	global_load_dwordx4 v[252:255], v251, s[88:89]
	global_load_dwordx4 v[252:255], v251, s[88:89] offset:64
	global_load_dwordx4 v[252:255], v251, s[88:89] offset:128
	global_load_dwordx4 v[252:255], v251, s[88:89] offset:1536
	global_load_dwordx4 v[252:255], v251, s[88:89] offset:1600
	global_load_dwordx4 v[252:255], v251, s[88:89] offset:1664
	s_load_dword s0, s[0:1], 0x88
	s_lshl_b32 s1, s45, 6
	s_and_b32 s1, s1, 0xfffffe00
	s_or_b32 s2, s1, s44
	v_readfirstlane_b32 s4, v0
	s_waitcnt lgkmcnt(0)
	s_mul_i32 s3, s0, 0x60000
	s_mul_hi_i32 s1, s0, 0x60000
	s_add_u32 s3, s28, s3
	s_mulk_i32 s0, 0x300
	s_addc_u32 s5, s29, s1
	s_ashr_i32 s1, s0, 31
	s_lshl_b64 s[0:1], s[0:1], 2
	s_add_u32 s0, s30, s0
	s_addc_u32 s1, s31, s1
	s_lshr_b32 s6, s4, 6
	s_and_b32 s25, s25, 0xffff
	s_mul_i32 s4, s6, 0x6000
	v_and_b32_e32 v2, 63, v0
	s_mul_hi_u32 s7, s6, 0x6000
	s_add_u32 s4, s3, s4
	s_addc_u32 s5, s5, s7
	v_lshlrev_b32_e32 v56, 4, v2
	v_mov_b32_e32 v57, 0
	v_lshl_add_u64 v[54:55], s[4:5], 0, v[56:57]
	s_movk_i32 s3, 0x1000
	v_add_co_u32_e32 v50, vcc, s3, v54
	s_movk_i32 s3, 0x2000
	s_nop 0
	v_addc_co_u32_e32 v51, vcc, 0, v55, vcc
	v_add_co_u32_e32 v52, vcc, s3, v54
	global_load_dwordx4 v[2:5], v56, s[4:5] offset:1024
	global_load_dwordx4 v[6:9], v56, s[4:5] offset:2048
	v_addc_co_u32_e32 v53, vcc, 0, v55, vcc
	global_load_dwordx4 v[10:13], v56, s[4:5] offset:3072
	global_load_dwordx4 v[14:17], v[52:53], off offset:-4096
	global_load_dwordx4 v[18:21], v[50:51], off offset:1024
	global_load_dwordx4 v[22:25], v[50:51], off offset:2048
	global_load_dwordx4 v[26:29], v56, s[4:5]
	global_load_dwordx4 v[30:33], v[50:51], off offset:3072
	global_load_dwordx4 v[34:37], v[52:53], off
	global_load_dwordx4 v[38:41], v[52:53], off offset:1024
	global_load_dwordx4 v[42:45], v[52:53], off offset:2048
	global_load_dwordx4 v[46:49], v[52:53], off offset:3072
	s_movk_i32 s3, 0x3000
	v_add_co_u32_e32 v58, vcc, s3, v54
	s_movk_i32 s3, 0x4000
	s_nop 0
	v_addc_co_u32_e32 v59, vcc, 0, v55, vcc
	v_add_co_u32_e32 v140, vcc, s3, v54
	s_nop 1
	v_addc_co_u32_e32 v141, vcc, 0, v55, vcc
	s_barrier
	s_cmp_lt_u32 s94, 4
	s_cbranch_scc1 .Lmystag4_1
	s_sleep 4

_Z7k_stageILi0ELi4EEv8AttnArgsPKDF16_PKfPDF16_iii:
	s_load_dwordx2 s[86:87], s[0:1], 0x78
	s_load_dwordx2 s[82:83], s[0:1], 0x88
	s_mov_b32 s81, s3
	s_load_dwordx16 s[64:79], s[0:1], 0x0
	v_readfirstlane_b32 s94, v0
	s_nop 0
	s_lshr_b32 s94, s94, 6
	s_load_dwordx4 s[8:11], s[0:1], 0x70
	s_load_dwordx2 s[20:21], s[0:1], 0x80
	s_load_dwordx4 s[12:15], s[0:1], 0x88
	s_lshl_b32 s5, s2, 5
	s_waitcnt lgkmcnt(0)
	s_and_b32 s15, s5, 0xe0
	s_lshr_b32 s5, s2, 3
	s_add_i32 s15, s15, s5
	s_and_b32 s2, s2, 56
	v_readfirstlane_b32 s4, v0
	v_and_b32_e32 v1, 15, v0
	s_cmp_lt_i32 s14, 1
	v_bfe_u32 v158, v0, 4, 2
	s_cbranch_scc1 .LBB5_79
	s_bfe_u32 s5, s4, 0x10006
	s_lshl_b32 s6, s5, 4
	s_mul_i32 s16, s3, 40
	s_mul_hi_i32 s7, s3, 40
	s_add_u32 s22, s0, s16
	s_addc_u32 s23, s1, s7
	s_load_dwordx4 s[16:19], s[22:23], 0x0
	s_load_dwordx2 s[0:1], s[22:23], 0x10
	v_or_b32_e32 v159, s6, v1
	v_lshlrev_b32_e32 v18, 5, v159
	s_waitcnt lgkmcnt(0)
	global_load_dwordx4 v[230:233], v18, s[18:19]
	global_load_dwordx4 v[234:237], v18, s[0:1]
	global_load_dwordx4 v[238:241], v18, s[18:19] offset:16
	global_load_dwordx4 v[242:245], v18, s[0:1] offset:16
	v_bfe_u32 v21, v0, 7, 1
	v_lshrrev_b32_e32 v19, 4, v0
	v_lshlrev_b16_e32 v23, 2, v21
	v_lshrrev_b32_e32 v18, 5, v0
	v_lshrrev_b32_e32 v20, 6, v0
	v_and_b32_e32 v24, 3, v19
	v_bitop3_b16 v19, v23, v19, 3 bitop3:0xf8
	s_movk_i32 s0, 0x3000
	v_and_b32_e32 v18, 4, v18
	v_and_b32_e32 v22, 4, v20
	v_lshlrev_b32_e32 v20, 12, v20
	v_lshlrev_b32_e32 v21, 11, v21
	v_and_b32_e32 v19, 0xffff, v19
	s_bitcmp1_b32 s4, 6
	v_or_b32_e32 v161, v18, v158
	v_and_or_b32 v162, s15, 56, v22
	v_bitop3_b16 v23, v23, 8, v24 bitop3:0xfe
	v_lshlrev_b32_e32 v24, 3, v22
	v_lshl_or_b32 v22, v22, 12, v21
	v_or3_b32 v163, v20, v21, s0
	v_bitop3_b32 v18, v18, v159, v158 bitop3:0x36
	v_bitop3_b32 v19, s6, v19, v1 bitop3:0x36
	s_cselect_b64 s[24:25], -1, 0
	s_and_b32 s0, s15, 0x1ffc0
	s_movk_i32 s1, 0x2000
	v_lshl_or_b32 v168, v18, 4, v22
	v_lshlrev_b32_e32 v18, 4, v19
	v_or_b32_e32 v19, s0, v162
	v_add3_u32 v170, v22, v18, s1
	v_lshl_or_b32 v18, v19, 6, s2
	v_add_u32_e32 v18, v161, v18
	v_mul_u32_u24_e32 v18, 0x600, v18
	v_and_b32_e32 v20, 0xffff, v23
	v_lshl_or_b32 v18, s5, 8, v18
	v_lshlrev_b32_e32 v160, 9, v158
	v_bitop3_b32 v20, s6, v20, v1 bitop3:0x36
	v_lshl_or_b32 v18, v1, 4, v18
	v_add_u32_e32 v164, -1, v162
	v_add_u32_e32 v165, 4, v162
	v_or3_b32 v166, v161, v24, 8
	v_or_b32_e32 v167, 0x1000, v22
	v_lshl_or_b32 v169, v20, 4, v160
	s_and_b32 s17, s17, 0xffff
	s_mov_b32 s19, 0x20000
	s_mov_b32 s18, 0x1800000
	v_add_u32_e32 v171, 0xfffe7c00, v18
	s_mov_b32 s30, s2
	s_mov_b32 s93, 0
	s_branch .LBB5_4

.LBB5_79:
	s_mul_i32 s84, s81, s83
	s_add_i32 s84, s84, s82
	s_mul_i32 s84, s84, 0xc00
	s_add_u32 s88, s86, s84
	s_addc_u32 s89, s87, 0
	v_mbcnt_lo_u32_b32 v251, -1, 0
	v_mbcnt_hi_u32_b32 v251, -1, v251
	v_bfe_u32 v251, v251, 4, 2
	v_lshlrev_b32_e32 v251, 4, v251
	s_mul_i32 s85, s94, 0xc0
	v_add_u32_e32 v251, s85, v251
	global_load_dwordx4 v[252:255], v251, s[88:89]
	global_load_dwordx4 v[252:255], v251, s[88:89] offset:64
	global_load_dwordx4 v[252:255], v251, s[88:89] offset:128
	global_load_dwordx4 v[252:255], v251, s[88:89] offset:1536
	global_load_dwordx4 v[252:255], v251, s[88:89] offset:1600
	global_load_dwordx4 v[252:255], v251, s[88:89] offset:1664
	s_mul_i32 s0, s13, s3
	s_lshl_b32 s1, s15, 6
	s_add_i32 s0, s0, s12
	s_and_b32 s1, s1, 0xfffffe00
	s_or_b32 s6, s1, s2
	s_mul_i32 s2, s0, 0x60000
	s_mul_hi_i32 s1, s0, 0x60000
	s_add_u32 s2, s8, s2
	s_mulk_i32 s0, 0x300
	s_addc_u32 s7, s9, s1
	s_ashr_i32 s1, s0, 31
	s_lshl_b64 s[0:1], s[0:1], 2
	s_add_u32 s4, s10, s0
	s_addc_u32 s5, s11, s1
	s_mul_i32 s0, s3, 0x1800000
	s_mul_hi_i32 s1, s3, 0x1800000
	s_add_u32 s0, s20, s0
	v_readfirstlane_b32 s3, v0
	s_addc_u32 s1, s21, s1
	s_lshr_b32 s8, s3, 6
	s_and_b32 s1, s1, 0xffff
	s_mul_i32 s9, s8, 0x6000
	v_and_b32_e32 v2, 63, v0
	s_mul_hi_u32 s3, s8, 0x6000
	s_add_u32 s2, s2, s9
	s_addc_u32 s3, s7, s3
	v_lshlrev_b32_e32 v56, 4, v2
	v_mov_b32_e32 v57, 0
	v_lshl_add_u64 v[54:55], s[2:3], 0, v[56:57]
	s_movk_i32 s7, 0x1000
	v_add_co_u32_e32 v50, vcc, s7, v54
	s_movk_i32 s7, 0x2000
	s_nop 0
	v_addc_co_u32_e32 v51, vcc, 0, v55, vcc
	v_add_co_u32_e32 v52, vcc, s7, v54
	global_load_dwordx4 v[2:5], v56, s[2:3] offset:1024
	global_load_dwordx4 v[6:9], v56, s[2:3] offset:2048
	v_addc_co_u32_e32 v53, vcc, 0, v55, vcc
	global_load_dwordx4 v[10:13], v56, s[2:3] offset:3072
	global_load_dwordx4 v[14:17], v[52:53], off offset:-4096
	global_load_dwordx4 v[18:21], v[50:51], off offset:1024
	global_load_dwordx4 v[22:25], v[50:51], off offset:2048
	global_load_dwordx4 v[26:29], v56, s[2:3]
	global_load_dwordx4 v[30:33], v[50:51], off offset:3072
	global_load_dwordx4 v[34:37], v[52:53], off
	global_load_dwordx4 v[38:41], v[52:53], off offset:1024
	global_load_dwordx4 v[42:45], v[52:53], off offset:2048
	global_load_dwordx4 v[46:49], v[52:53], off offset:3072
	s_movk_i32 s2, 0x3000
	v_add_co_u32_e32 v58, vcc, s2, v54
	s_movk_i32 s2, 0x4000
	s_nop 0
	v_addc_co_u32_e32 v59, vcc, 0, v55, vcc
	v_add_co_u32_e32 v140, vcc, s2, v54
	s_waitcnt lgkmcnt(0)
	s_nop 0
	v_addc_co_u32_e32 v141, vcc, 0, v55, vcc
	s_barrier
	s_cmp_lt_u32 s94, 4
	s_cbranch_scc1 .Lmystag5_1
	s_sleep 4

amdhsa.kernels:
  - .agpr_count:     0
    .args:
      - .actual_access:  read_only
        .address_space:  global
        .offset:         0
        .size:           8
        .value_kind:     global_buffer
      - .actual_access:  read_only
        .address_space:  global
        .offset:         8
        .size:           8
        .value_kind:     global_buffer
      - .actual_access:  read_only
        .address_space:  global
        .offset:         16
        .size:           8
        .value_kind:     global_buffer
      - .actual_access:  read_only
        .address_space:  global
        .offset:         24
        .size:           8
        .value_kind:     global_buffer
      - .actual_access:  read_only
        .address_space:  global
        .offset:         32
        .size:           8
        .value_kind:     global_buffer
      - .actual_access:  read_only
        .address_space:  global
        .offset:         40
        .size:           8
        .value_kind:     global_buffer
      - .actual_access:  read_only
        .address_space:  global
        .offset:         48
        .size:           8
        .value_kind:     global_buffer
      - .actual_access:  read_only
        .address_space:  global
        .offset:         56
        .size:           8
        .value_kind:     global_buffer
      - .actual_access:  write_only
        .address_space:  global
        .offset:         64
        .size:           8
        .value_kind:     global_buffer
      - .actual_access:  write_only
        .address_space:  global
        .offset:         72
        .size:           8
        .value_kind:     global_buffer
      - .actual_access:  write_only
        .address_space:  global
        .offset:         80
        .size:           8
        .value_kind:     global_buffer
      - .actual_access:  write_only
        .address_space:  global
        .offset:         88
        .size:           8
        .value_kind:     global_buffer
    .group_segment_fixed_size: 0
    .kernarg_segment_align: 8
    .kernarg_segment_size: 96
    .language:       OpenCL C
    .language_version:
      - 2
      - 0
    .max_flat_workgroup_size: 256
    .name:           _Z8k_prep_wPKfS0_S0_S0_S0_S0_S0_S0_PDF16_PfS1_S1_
    .private_segment_fixed_size: 0
    .sgpr_count:     23
    .sgpr_spill_count: 0
    .symbol:         _Z8k_prep_wPKfS0_S0_S0_S0_S0_S0_S0_PDF16_PfS1_S1_.kd
    .uniform_work_group_size: 1
    .uses_dynamic_stack: false
    .vgpr_count:     15
    .vgpr_spill_count: 0
    .wavefront_size: 64
  - .agpr_count:     0
    .args:
      - .actual_access:  read_only
        .address_space:  global
        .offset:         0
        .size:           8
        .value_kind:     global_buffer
      - .actual_access:  read_only
        .address_space:  global
        .offset:         8
        .size:           8
        .value_kind:     global_buffer
      - .actual_access:  read_only
        .address_space:  global
        .offset:         16
        .size:           8
        .value_kind:     global_buffer
      - .actual_access:  read_only
        .address_space:  global
        .offset:         24
        .size:           8
        .value_kind:     global_buffer
      - .actual_access:  write_only
        .address_space:  global
        .offset:         32
        .size:           8
        .value_kind:     global_buffer
      - .actual_access:  read_only
        .address_space:  global
        .offset:         40
        .size:           8
        .value_kind:     global_buffer
      - .actual_access:  read_only
        .address_space:  global
        .offset:         48
        .size:           8
        .value_kind:     global_buffer
      - .actual_access:  write_only
        .address_space:  global
        .offset:         56
        .size:           8
        .value_kind:     global_buffer
      - .offset:         64
        .size:           4
        .value_kind:     by_value
      - .offset:         68
        .size:           4
        .value_kind:     by_value
    .group_segment_fixed_size: 115712
    .kernarg_segment_align: 8
    .kernarg_segment_size: 72
    .language:       OpenCL C
    .language_version:
      - 2
      - 0
    .max_flat_workgroup_size: 512
    .name:           _Z8k_stageAPKfS0_S0_S0_PDF16_PKDF16_S0_S1_ii
    .private_segment_fixed_size: 0
    .sgpr_count:     28
    .sgpr_spill_count: 0
    .symbol:         _Z8k_stageAPKfS0_S0_S0_PDF16_PKDF16_S0_S1_ii.kd
    .uniform_work_group_size: 1
    .uses_dynamic_stack: false
    .vgpr_count:     256
    .vgpr_spill_count: 0
    .wavefront_size: 64
  - .agpr_count:     112
    .args:
      - .actual_access:  read_only
        .address_space:  global
        .offset:         0
        .size:           8
        .value_kind:     global_buffer
      - .actual_access:  read_only
        .address_space:  global
        .offset:         8
        .size:           8
        .value_kind:     global_buffer
      - .actual_access:  read_only
        .address_space:  global
        .offset:         16
        .size:           8
        .value_kind:     global_buffer
      - .actual_access:  read_only
        .address_space:  global
        .offset:         24
        .size:           8
        .value_kind:     global_buffer
      - .actual_access:  read_only
        .address_space:  global
        .offset:         32
        .size:           8
        .value_kind:     global_buffer
      - .actual_access:  write_only
        .address_space:  global
        .offset:         40
        .size:           8
        .value_kind:     global_buffer
    .group_segment_fixed_size: 107712
    .kernarg_segment_align: 8
    .kernarg_segment_size: 48
    .language:       OpenCL C
    .language_version:
      - 2
      - 0
    .max_flat_workgroup_size: 256
    .name:           _Z7k_conv4PKDF16_S0_S0_PKfS2_Pf
    .private_segment_fixed_size: 0
    .sgpr_count:     36
    .sgpr_spill_count: 0
    .symbol:         _Z7k_conv4PKDF16_S0_S0_PKfS2_Pf.kd
    .uniform_work_group_size: 1
    .uses_dynamic_stack: false
    .vgpr_count:     328
    .vgpr_spill_count: 0
    .wavefront_size: 64
  - .agpr_count:     0
    .args:
      - .offset:         0
        .size:           112
        .value_kind:     by_value
      - .actual_access:  read_only
        .address_space:  global
        .offset:         112
        .size:           8
        .value_kind:     global_buffer
      - .actual_access:  read_only
        .address_space:  global
        .offset:         120
        .size:           8
        .value_kind:     global_buffer
      - .actual_access:  write_only
        .address_space:  global
        .offset:         128
        .size:           8
        .value_kind:     global_buffer
      - .offset:         136
        .size:           4
        .value_kind:     by_value
      - .offset:         140
        .size:           4
        .value_kind:     by_value
      - .offset:         144
        .size:           4
        .value_kind:     by_value
    .group_segment_fixed_size: 115712
    .kernarg_segment_align: 8
    .kernarg_segment_size: 148
    .language:       OpenCL C
    .language_version:
      - 2
      - 0
    .max_flat_workgroup_size: 512
    .name:           _Z7k_stageILi0ELi8EEv8AttnArgsPKDF16_PKfPDF16_iii
    .private_segment_fixed_size: 0
    .sgpr_count:     41
    .sgpr_spill_count: 0
    .symbol:         _Z7k_stageILi0ELi8EEv8AttnArgsPKDF16_PKfPDF16_iii.kd
    .uniform_work_group_size: 1
    .uses_dynamic_stack: false
    .vgpr_count:     256
    .vgpr_spill_count: 0
    .wavefront_size: 64
  - .agpr_count:     0
    .args:
      - .offset:         0
        .size:           112
        .value_kind:     by_value
      - .actual_access:  read_only
        .address_space:  global
        .offset:         112
        .size:           8
        .value_kind:     global_buffer
      - .actual_access:  read_only
        .address_space:  global
        .offset:         120
        .size:           8
        .value_kind:     global_buffer
      - .actual_access:  write_only
        .address_space:  global
        .offset:         128
        .size:           8
        .value_kind:     global_buffer
      - .offset:         136
        .size:           4
        .value_kind:     by_value
      - .offset:         140
        .size:           4
        .value_kind:     by_value
      - .offset:         144
        .size:           4
        .value_kind:     by_value
    .group_segment_fixed_size: 82944
    .kernarg_segment_align: 8
    .kernarg_segment_size: 148
    .language:       OpenCL C
    .language_version:
      - 2
      - 0
    .max_flat_workgroup_size: 512
    .name:           _Z7k_stageILi1ELi4EEv8AttnArgsPKDF16_PKfPDF16_iii
    .private_segment_fixed_size: 0
    .sgpr_count:     55
    .sgpr_spill_count: 0
    .symbol:         _Z7k_stageILi1ELi4EEv8AttnArgsPKDF16_PKfPDF16_iii.kd
    .uniform_work_group_size: 1
    .uses_dynamic_stack: false
    .vgpr_count:     256
    .vgpr_spill_count: 0
    .wavefront_size: 64
  - .agpr_count:     0
    .args:
      - .offset:         0
        .size:           112
        .value_kind:     by_value
      - .actual_access:  read_only
        .address_space:  global
        .offset:         112
        .size:           8
        .value_kind:     global_buffer
      - .actual_access:  read_only
        .address_space:  global
        .offset:         120
        .size:           8
        .value_kind:     global_buffer
      - .actual_access:  write_only
        .address_space:  global
        .offset:         128
        .size:           8
        .value_kind:     global_buffer
      - .offset:         136
        .size:           4
        .value_kind:     by_value
      - .offset:         140
        .size:           4
        .value_kind:     by_value
      - .offset:         144
        .size:           4
        .value_kind:     by_value
    .group_segment_fixed_size: 82944
    .kernarg_segment_align: 8
    .kernarg_segment_size: 148
    .language:       OpenCL C
    .language_version:
      - 2
      - 0
    .max_flat_workgroup_size: 512
    .name:           _Z7k_stageILi0ELi4EEv8AttnArgsPKDF16_PKfPDF16_iii
    .private_segment_fixed_size: 0
    .sgpr_count:     38
    .sgpr_spill_count: 0
    .symbol:         _Z7k_stageILi0ELi4EEv8AttnArgsPKDF16_PKfPDF16_iii.kd
    .uniform_work_group_size: 1
    .uses_dynamic_stack: false
    .vgpr_count:     256
    .vgpr_spill_count: 0
    .wavefront_size: 64
  - .agpr_count:     0
    .args:
      - .offset:         0
        .size:           112
        .value_kind:     by_value
    .group_segment_fixed_size: 0
    .kernarg_segment_align: 8
    .kernarg_segment_size: 112
    .language:       OpenCL C
    .language_version:
      - 2
      - 0
    .max_flat_workgroup_size: 512
    .name:           _Z7k_attn2ILi2EEv8AttnArgs
    .private_segment_fixed_size: 0
    .sgpr_count:     102
    .sgpr_spill_count: 0
    .symbol:         _Z7k_attn2ILi2EEv8AttnArgs.kd
    .uniform_work_group_size: 1
    .uses_dynamic_stack: false
    .vgpr_count:     252
    .vgpr_spill_count: 0
    .wavefront_size: 64
